# hybrid K1: per-wave regions as in the baseline; the last 4 of each region's 18 chunks form the shared pool, handed out in a scattered order (in-flight addresses span the whole matrix); flush spread ov
# baseline (speedup 1.0000x reference)
.Lk1_scan:
	s_load_dwordx2 s[4:5], s[0:1], 0x0
	s_load_dwordx4 s[8:11], s[0:1], 0x20
	s_load_dwordx2 s[12:13], s[0:1], 0x30
	v_and_b32_e32 v6, 63, v0
	v_readfirstlane_b32 s3, v0
	v_lshlrev_b32_e32 v1, 4, v6
	v_lshlrev_b32_e32 v2, 2, v6
	v_or_b32_e32 v3, 1, v2
	v_or_b32_e32 v4, 2, v2
	v_or_b32_e32 v5, 3, v2
	s_lshr_b32 s3, s3, 6
	s_sub_u32 s16, s2, 0x60
	s_lshl_b32 s16, s16, 2
	s_add_u32 s16, s16, s3
	s_mul_i32 s17, s16, 0x48000
	s_lshr_b32 s18, s17, 2
	s_lshl_b32 s24, s3, 13
	s_mov_b32 s25, s24
	s_mov_b32 s28, s24
	s_mov_b32 s36, 0
	v_mov_b32_e32 v21, 1
	s_mov_b32 s27, 0
	s_mov_b32 s29, 0x55555556
	s_mov_b32 s31, 0xc0000
	s_waitcnt lgkmcnt(0)
	s_and_b32 s50, s16, 15
	s_mul_i32 s52, s50, 512
	s_add_u32 s52, s52, 28672
	s_lshl_b32 s53, s50, 6
	s_add_u32 s53, s53, 0xe000
	s_add_u32 s54, s10, s53
	s_addc_u32 s55, s11, 0
	s_mul_i32 s59, s16, 18
	s_mul_i32 s57, s59, 0x4000
	s_lshr_b32 s18, s57, 2
	s_add_u32 s6, s4, s57
	s_addc_u32 s7, s5, 0
	v_mov_b32_e32 v27, 0
	global_load_dwordx4 v[28:31], v1, s[6:7] nt
	s_add_u32 s6, s6, 0x400
	s_addc_u32 s7, s7, 0
	global_load_dwordx4 v[32:35], v1, s[6:7] nt
	s_add_u32 s6, s6, 0x400
	s_addc_u32 s7, s7, 0
	global_load_dwordx4 v[36:39], v1, s[6:7] nt
	s_add_u32 s6, s6, 0x400
	s_addc_u32 s7, s7, 0
	global_load_dwordx4 v[40:43], v1, s[6:7] nt
	s_add_u32 s6, s6, 0x400
	s_addc_u32 s7, s7, 0
	global_load_dwordx4 v[44:47], v1, s[6:7] nt
	s_add_u32 s6, s6, 0x400
	s_addc_u32 s7, s7, 0
	global_load_dwordx4 v[48:51], v1, s[6:7] nt
	s_add_u32 s6, s6, 0x400
	s_addc_u32 s7, s7, 0
	global_load_dwordx4 v[52:55], v1, s[6:7] nt
	s_add_u32 s6, s6, 0x400
	s_addc_u32 s7, s7, 0
	global_load_dwordx4 v[56:59], v1, s[6:7] nt
	s_add_u32 s6, s6, 0x400
	s_addc_u32 s7, s7, 0
	global_load_dwordx4 v[60:63], v1, s[6:7] nt
	s_add_u32 s6, s6, 0x400
	s_addc_u32 s7, s7, 0
	global_load_dwordx4 v[64:67], v1, s[6:7] nt
	s_add_u32 s6, s6, 0x400
	s_addc_u32 s7, s7, 0
	global_load_dwordx4 v[68:71], v1, s[6:7] nt
	s_add_u32 s6, s6, 0x400
	s_addc_u32 s7, s7, 0
	global_load_dwordx4 v[72:75], v1, s[6:7] nt
	s_add_u32 s6, s6, 0x400
	s_addc_u32 s7, s7, 0
	global_load_dwordx4 v[76:79], v1, s[6:7] nt
	s_add_u32 s6, s6, 0x400
	s_addc_u32 s7, s7, 0
	global_load_dwordx4 v[80:83], v1, s[6:7] nt
	s_add_u32 s6, s6, 0x400
	s_addc_u32 s7, s7, 0
	global_load_dwordx4 v[84:87], v1, s[6:7] nt
	s_add_u32 s6, s6, 0x400
	s_addc_u32 s7, s7, 0
	global_load_dwordx4 v[88:91], v1, s[6:7] nt
	s_add_u32 s6, s6, 0x400
	s_addc_u32 s7, s7, 0
	s_mov_b32 s26, 18
	s_add_u32 s57, s59, 1
	s_mul_i32 s57, s57, 0x4000
	s_lshr_b32 s58, s57, 2
	s_add_u32 s6, s4, s57
	s_addc_u32 s7, s5, 0
	s_mov_b32 s26, 0

.Lk1_dynid:
	v_readfirstlane_b32 s56, v26
	s_nop 0
	s_cmp_lt_u32 s56, 512
	s_cbranch_scc0 .Lk1_lastchunk
	s_lshl_b32 s57, s56, 4
	s_add_u32 s57, s57, s50
	s_lshr_b32 s61, s57, 11
	s_mul_i32 s57, s57, 1021
	s_and_b32 s57, s57, 2047
	s_mul_i32 s57, s57, 18
	s_add_u32 s57, s57, s61
	s_add_u32 s57, s57, 14
